# v57 + LN1 router logits: 52 of 64 product chunks as 4 v_fmac into the expert accumulator (was mul+fmac, mul+fmac, add, add)
# speedup vs baseline: 1.0003x; 1.0003x over previous
; __device__ __forceinline__ unsigned pk2(float lo, float hi) { return (unsigned)f2bf(lo) | ((unsigned)f2bf(hi) << 16); }
; __device__ __forceinline__ float frsq(float x) { return __builtin_amdgcn_rsqf(x); }
; __device__ __forceinline__ void ln_affine(f32x4 (&v)[4], const LnPar& q) {
;     float s = 0.f;
; #pragma unroll
;     for (int j = 0; j < 4; ++j) s += (v[j][0] + v[j][1]) + (v[j][2] + v[j][3]);
;     const float mean = wave_sum(s) * (1.f / D); float s2 = 0.f;
; #pragma unroll
;     for (int j = 0; j < 4; ++j) { v[j] = v[j] - mean; s2 += (v[j][0] * v[j][0] + v[j][1] * v[j][1]) + (v[j][2] * v[j][2] + v[j][3] * v[j][3]); }
;     const float rstd = frsq(wave_sum(s2) * (1.f / D) + 1e-5f);
; #pragma unroll
;     for (int j = 0; j < 4; ++j) v[j] = v[j] * rstd * q.g[j] + q.b[j];
; }
; __device__ __forceinline__ void store_row_bf16(bf16_t* row, const f32x4 (&v)[4], int lane) {
; #pragma unroll
;     for (int j = 0; j < 4; ++j) { u32x2 w; w.x = pk2(v[j][0], v[j][1]); w.y = pk2(v[j][2], v[j][3]); *(u32x2*)(row + 4 * lane + 256 * j) = w; }
; }
; __device__ __forceinline__ void ph_ln1(const Params& p, int l, LAS unsigned char* lds, const int wvid) {
;     ...
;         ln_affine(v, ln1);
;         store_row_bf16(HB + (size_t)r * D, v, lane);
.LBB0_1078:
	s_or_b64 exec, exec, s[0:1]
	v_pk_add_f32 v[64:65], v[66:67], v[34:35]
	v_add_f32_e32 v75, v62, v63
	v_add_f32_e32 v0, v64, v65
	v_pk_add_f32 v[64:65], v[68:69], v[36:37]
	v_add_f32_e32 v77, 0, v0
	v_pk_add_f32 v[64:65], v[64:65], v[64:65] op_sel_hi:[0,1]
	v_add_f32_e32 v79, v60, v61
	v_mov_b32_e32 v73, v65
	v_pk_add_f32 v[70:71], v[74:75], v[78:79]
	v_pk_add_f32 v[64:65], v[72:73], v[76:77]
	ds_read_b128 v[118:121], v39
	ds_read_b128 v[122:125], v39 offset:4096
	ds_read_b128 v[126:129], v39 offset:8192
	ds_read_b128 v[130:133], v39 offset:12288
	ds_read_b128 v[134:137], v39 offset:16384
	ds_read_b128 v[138:141], v39 offset:20480
	ds_read_b128 v[142:145], v39 offset:24576
	ds_read_b128 v[146:149], v39 offset:28672
	ds_read_b128 v[232:235], v39 offset:32768
	ds_read_b128 v[236:239], v39 offset:36864
	ds_read_b128 v[240:243], v39 offset:40960
	ds_read_b128 v[244:247], v39 offset:45056
	v_pk_add_f32 v[64:65], v[70:71], v[64:65]
	s_nop 0
	v_add_f32_e32 v0, v64, v65
	v_mov_b32_e32 v64, v1
	s_nop 0
	v_add_f32_dpp v0, v0, v0 quad_perm:[1,0,3,2] row_mask:0xf bank_mask:0xf bound_ctrl:1
	s_nop 1
	v_add_f32_dpp v0, v0, v0 quad_perm:[2,3,0,1] row_mask:0xf bank_mask:0xf bound_ctrl:1
	s_nop 1
	v_add_f32_dpp v0, v0, v0 row_half_mirror row_mask:0xf bank_mask:0xf bound_ctrl:1
	s_nop 1
	v_add_f32_dpp v0, v0, v0 row_mirror row_mask:0xf bank_mask:0xf bound_ctrl:1
	s_nop 1
	v_mov_b32_dpp v64, v0 row_bcast:15 row_mask:0xa bank_mask:0xf
	v_add_f32_e32 v0, v0, v64
	v_mov_b32_e32 v64, v1
	s_nop 1
	v_mov_b32_dpp v64, v0 row_bcast:31 row_mask:0xc bank_mask:0xf
	v_add_f32_e32 v0, v0, v64
	s_nop 0
	v_readlane_b32 s0, v0, 63
	s_nop 1
	v_fmac_f32_e32 v66, s0, v220
	v_fmac_f32_e32 v35, s0, v220
	v_fmac_f32_e32 v67, s0, v220
	v_fmac_f32_e32 v34, s0, v220
	v_mov_b32_e32 v64, v67
	v_mov_b32_e32 v65, v35
	v_mov_b32_e32 v35, v66
	v_pk_mul_f32 v[70:71], v[64:65], v[64:65]
	v_pk_mul_f32 v[66:67], v[34:35], v[34:35]
	v_fmac_f32_e32 v68, s0, v220
	v_fmac_f32_e32 v37, s0, v220
	v_fmac_f32_e32 v69, s0, v220
	v_pk_mov_b32 v[80:81], v[66:67], v[70:71] op_sel:[1,0]
	v_mov_b32_e32 v67, v71
	v_fmac_f32_e32 v36, s0, v220
	v_mov_b32_e32 v70, v69
	v_mov_b32_e32 v71, v37
	v_mov_b32_e32 v37, v68
	v_pk_add_f32 v[66:67], v[80:81], v[66:67]
	v_pk_mul_f32 v[80:81], v[70:71], v[70:71]
	v_pk_mul_f32 v[68:69], v[36:37], v[36:37]
	v_fmac_f32_e32 v62, s0, v220
	v_pk_mov_b32 v[82:83], v[68:69], v[80:81] op_sel:[1,0]
	v_mov_b32_e32 v69, v81
	v_fmac_f32_e32 v63, s0, v220
	v_fmac_f32_e32 v60, s0, v220
	v_mul_f32_e32 v0, v62, v62
	v_pk_add_f32 v[68:69], v[82:83], v[68:69]
	v_fmac_f32_e32 v61, s0, v220
	v_pk_fma_f32 v[80:81], v[62:63], v[62:63], v[0:1] op_sel_hi:[1,1,0]
	v_mul_f32_e32 v0, v60, v60
	v_pk_add_f32 v[66:67], v[66:67], v[66:67] op_sel_hi:[0,1]
	v_pk_add_f32 v[68:69], v[68:69], v[68:69] op_sel_hi:[0,1]
	v_pk_fma_f32 v[82:83], v[60:61], v[60:61], v[0:1] op_sel_hi:[1,1,0]
	v_fmac_f32_e32 v76, s0, v220
	v_fmac_f32_e32 v72, s0, v220
	v_fmac_f32_e32 v78, s0, v220
	v_fmac_f32_e32 v74, s0, v220
	v_mul_f32_e32 v80, v74, v74
	v_mul_f32_e32 v82, v78, v78
	v_mul_f32_e32 v66, v72, v72
	v_mul_f32_e32 v68, v76, v76
	v_pk_add_f32 v[80:81], v[80:81], v[82:83]
	v_pk_add_f32 v[66:67], v[66:67], v[68:69]
	v_mov_b32_e32 v75, v78
	v_pk_add_f32 v[66:67], v[80:81], v[66:67]
	v_mov_b32_e32 v73, v76
	v_add_f32_e32 v0, v66, v67
	v_mov_b32_e32 v66, v1
	s_nop 0
	v_add_f32_dpp v0, v0, v0 quad_perm:[1,0,3,2] row_mask:0xf bank_mask:0xf bound_ctrl:1
	s_nop 1
	v_add_f32_dpp v0, v0, v0 quad_perm:[2,3,0,1] row_mask:0xf bank_mask:0xf bound_ctrl:1
	s_nop 1
	v_add_f32_dpp v0, v0, v0 row_half_mirror row_mask:0xf bank_mask:0xf bound_ctrl:1
	s_nop 1
	v_add_f32_dpp v0, v0, v0 row_mirror row_mask:0xf bank_mask:0xf bound_ctrl:1
	s_nop 1
	v_mov_b32_dpp v66, v0 row_bcast:15 row_mask:0xa bank_mask:0xf
	v_add_f32_e32 v0, v0, v66
	v_mov_b32_e32 v66, v1
	s_nop 1
	v_mov_b32_dpp v66, v0 row_bcast:31 row_mask:0xc bank_mask:0xf
	v_add_f32_e32 v0, v0, v66
	s_nop 0
	v_readlane_b32 s0, v0, 63
	s_nop 1
	v_fma_f32 v0, s0, v221, v204
	v_rsq_f32_e32 v0, v0
	s_nop 0
	v_pk_mul_f32 v[34:35], v[34:35], v[0:1] op_sel_hi:[1,0]
	s_nop 0
	v_pk_fma_f32 v[94:95], v[30:31], v[34:35], v[22:23]
	v_pk_mul_f32 v[34:35], v[36:37], v[0:1] op_sel_hi:[1,0]
	v_pk_mul_f32 v[36:37], v[70:71], v[0:1] op_sel_hi:[1,0]
	v_pk_mul_f32 v[64:65], v[64:65], v[0:1] op_sel_hi:[1,0]
	v_pk_fma_f32 v[68:69], v[28:29], v[36:37], v[20:21]
	v_pk_fma_f32 v[70:71], v[26:27], v[34:35], v[18:19]
	v_pk_mul_f32 v[34:35], v[62:63], v[0:1] op_sel_hi:[1,0]
	v_pk_mul_f32 v[36:37], v[60:61], v[0:1] op_sel_hi:[1,0]
	v_pk_fma_f32 v[92:93], v[32:33], v[64:65], v[24:25]
	v_pk_fma_f32 v[64:65], v[16:17], v[36:37], v[8:9]
	v_pk_fma_f32 v[66:67], v[14:15], v[34:35], v[6:7]
	v_pk_mul_f32 v[34:35], v[74:75], v[0:1] op_sel_hi:[1,0]
	v_pk_mul_f32 v[36:37], v[72:73], v[0:1] op_sel_hi:[1,0]
	v_bfe_u32 v0, v94, 16, 1
	v_pk_fma_f32 v[62:63], v[10:11], v[34:35], v[2:3]
	v_add3_u32 v0, v94, v0, s79
	v_bfe_u32 v34, v95, 16, 1
	v_lshrrev_b32_e32 v0, 16, v0
	v_add3_u32 v34, v95, v34, s79
	v_and_or_b32 v34, v34, s89, v0
	v_cvt_pk_bf16_f32 v35, v92, v93
	v_bfe_u32 v0, v70, 16, 1
	global_store_dwordx2 v[58:59], v[34:35], off offset:-1536
	v_add3_u32 v0, v70, v0, s79
	v_bfe_u32 v34, v71, 16, 1
	v_lshrrev_b32_e32 v0, 16, v0
	v_add3_u32 v34, v71, v34, s79
	v_and_or_b32 v34, v34, s89, v0
	v_cvt_pk_bf16_f32 v35, v68, v69
	v_bfe_u32 v0, v66, 16, 1
	global_store_dwordx2 v[58:59], v[34:35], off offset:-1024
	v_add3_u32 v0, v66, v0, s79
	v_bfe_u32 v34, v67, 16, 1
	v_lshrrev_b32_e32 v0, 16, v0
	v_add3_u32 v34, v67, v34, s79
	v_and_or_b32 v34, v34, s89, v0
	v_cvt_pk_bf16_f32 v35, v64, v65
	v_bfe_u32 v0, v62, 16, 1
	global_store_dwordx2 v[58:59], v[34:35], off offset:-512
	v_add3_u32 v0, v62, v0, s79
	v_bfe_u32 v34, v63, 16, 1
	v_pk_fma_f32 v[60:61], v[12:13], v[36:37], v[4:5]
	v_lshrrev_b32_e32 v0, 16, v0
	v_add3_u32 v34, v63, v34, s79
	v_and_or_b32 v34, v34, s89, v0
	v_cvt_pk_bf16_f32 v35, v60, v61
	global_store_dwordx2 v[58:59], v[34:35], off
	s_waitcnt lgkmcnt(11)
; #define LAS __attribute__((address_space(3)))
; __device__ __forceinline__ void ph_ln1(const Params& p, int l, LAS unsigned char* lds, const int wvid) {
;     ...
; #pragma unroll
;         for (int j = 0; j < 4; ++j)
; #pragma unroll
;             for (int e = 0; e < 16; ++e) { const f32x4 w = *(const LAS f32x4*)(rw + e * D + 256 * j + 4 * lane);
;                 lg[e] += (v[j][0] * w[0] + v[j][1] * w[1]) + (v[j][2] * w[2] + v[j][3] * w[3]); }
	v_mul_f32_e32 v72, v119, v95
	v_fmac_f32_e32 v72, v118, v94
	v_fmac_f32_e32 v72, v121, v93
	v_fmac_f32_e32 v72, v120, v92
	ds_read_b128 v[118:121], v39 offset:49152
	s_waitcnt lgkmcnt(11)
	v_mul_f32_e32 v73, v123, v95
	v_fmac_f32_e32 v73, v122, v94
	v_fmac_f32_e32 v73, v125, v93
	v_fmac_f32_e32 v73, v124, v92
	ds_read_b128 v[122:125], v39 offset:53248
	s_waitcnt lgkmcnt(11)
	v_mul_f32_e32 v75, v95, v127
	v_fmac_f32_e32 v75, v94, v126
	v_fmac_f32_e32 v75, v93, v129
	v_fmac_f32_e32 v75, v92, v128
	ds_read_b128 v[126:129], v39 offset:57344
	s_waitcnt lgkmcnt(11)
	v_mul_f32_e32 v77, v95, v131
	v_fmac_f32_e32 v77, v94, v130
	v_fmac_f32_e32 v77, v93, v133
	v_fmac_f32_e32 v77, v92, v132
	ds_read_b128 v[130:133], v39 offset:61440
	s_waitcnt lgkmcnt(11)
	v_mul_f32_e32 v79, v95, v135
	v_fmac_f32_e32 v79, v94, v134
	v_fmac_f32_e32 v79, v93, v137
	v_fmac_f32_e32 v79, v92, v136
	ds_read_b128 v[134:137], v39 offset:1024
	s_waitcnt lgkmcnt(11)
	v_mul_f32_e32 v81, v95, v139
	v_fmac_f32_e32 v81, v94, v138
	v_fmac_f32_e32 v81, v93, v141
	v_fmac_f32_e32 v81, v92, v140
	ds_read_b128 v[138:141], v39 offset:5120
	s_waitcnt lgkmcnt(11)
	v_mul_f32_e32 v82, v95, v143
	v_fmac_f32_e32 v82, v94, v142
	v_fmac_f32_e32 v82, v93, v145
	v_fmac_f32_e32 v82, v92, v144
	ds_read_b128 v[142:145], v39 offset:9216
	s_waitcnt lgkmcnt(11)
	v_mul_f32_e32 v80, v95, v147
	v_fmac_f32_e32 v80, v94, v146
	v_fmac_f32_e32 v80, v93, v149
	v_fmac_f32_e32 v80, v92, v148
	ds_read_b128 v[146:149], v39 offset:13312
	s_waitcnt lgkmcnt(11)
	v_mul_f32_e32 v78, v95, v233
	v_fmac_f32_e32 v78, v94, v232
	v_fmac_f32_e32 v78, v93, v235
	v_fmac_f32_e32 v78, v92, v234
	ds_read_b128 v[232:235], v39 offset:17408
	s_waitcnt lgkmcnt(11)
	v_mul_f32_e32 v76, v95, v237
	v_fmac_f32_e32 v76, v94, v236
	v_fmac_f32_e32 v76, v93, v239
	v_fmac_f32_e32 v76, v92, v238
	ds_read_b128 v[236:239], v39 offset:21504
	s_waitcnt lgkmcnt(11)
	v_mul_f32_e32 v74, v95, v241
	v_fmac_f32_e32 v74, v94, v240
	v_fmac_f32_e32 v74, v93, v243
	v_fmac_f32_e32 v74, v92, v242
	ds_read_b128 v[240:243], v39 offset:25600
	s_waitcnt lgkmcnt(11)
	v_mul_f32_e32 v37, v95, v245
	v_fmac_f32_e32 v37, v94, v244
	v_fmac_f32_e32 v37, v93, v247
	v_fmac_f32_e32 v37, v92, v246
	ds_read_b128 v[244:247], v39 offset:29696
	s_waitcnt lgkmcnt(11)
	v_mul_f32_e32 v36, v95, v119
	v_fmac_f32_e32 v36, v93, v121
	v_fmac_f32_e32 v36, v94, v118
	v_fmac_f32_e32 v36, v92, v120
	ds_read_b128 v[118:121], v39 offset:33792
	s_waitcnt lgkmcnt(11)
	v_mul_f32_e32 v35, v95, v123
	v_fmac_f32_e32 v35, v93, v125
	v_fmac_f32_e32 v35, v94, v122
	v_fmac_f32_e32 v35, v92, v124
	ds_read_b128 v[122:125], v39 offset:37888
	s_waitcnt lgkmcnt(11)
	v_mul_f32_e32 v0, v95, v127
	v_mul_f32_e32 v34, v93, v129
	v_fmac_f32_e32 v0, v94, v126
	v_fmac_f32_e32 v34, v92, v128
	ds_read_b128 v[126:129], v39 offset:41984
	v_add_f32_e32 v0, v0, v34
	v_add_f32_e32 v34, 0, v0
	s_waitcnt lgkmcnt(11)
	v_mul_f32_e32 v0, v95, v131
	v_mul_f32_e32 v83, v93, v133
	v_fmac_f32_e32 v0, v94, v130
	v_fmac_f32_e32 v83, v92, v132
	ds_read_b128 v[130:133], v39 offset:46080
	v_add_f32_e32 v0, v0, v83
	v_add_f32_e32 v0, 0, v0
	s_waitcnt lgkmcnt(11)
	v_fmac_f32_e32 v72, v71, v135
	v_fmac_f32_e32 v72, v70, v134
	v_fmac_f32_e32 v72, v69, v137
	v_fmac_f32_e32 v72, v68, v136
	ds_read_b128 v[134:137], v39 offset:50176
	s_waitcnt lgkmcnt(11)
	v_fmac_f32_e32 v73, v71, v139
	v_fmac_f32_e32 v73, v70, v138
	v_fmac_f32_e32 v73, v69, v141
	v_fmac_f32_e32 v73, v68, v140
	ds_read_b128 v[138:141], v39 offset:54272
	s_waitcnt lgkmcnt(11)
	v_fmac_f32_e32 v75, v71, v143
	v_fmac_f32_e32 v75, v70, v142
	v_fmac_f32_e32 v75, v69, v145
	v_fmac_f32_e32 v75, v68, v144
	ds_read_b128 v[142:145], v39 offset:58368
	s_waitcnt lgkmcnt(11)
	v_fmac_f32_e32 v77, v71, v147
	v_fmac_f32_e32 v77, v70, v146
	v_fmac_f32_e32 v77, v69, v149
	v_fmac_f32_e32 v77, v68, v148
	ds_read_b128 v[146:149], v39 offset:62464
	s_waitcnt lgkmcnt(11)
	v_fmac_f32_e32 v79, v71, v233
	v_fmac_f32_e32 v79, v70, v232
	v_fmac_f32_e32 v79, v69, v235
	v_fmac_f32_e32 v79, v68, v234
	ds_read_b128 v[232:235], v39 offset:2048
	s_waitcnt lgkmcnt(11)
	v_fmac_f32_e32 v81, v71, v237
	v_fmac_f32_e32 v81, v70, v236
	v_fmac_f32_e32 v81, v69, v239
	v_fmac_f32_e32 v81, v68, v238
	ds_read_b128 v[236:239], v39 offset:6144
	s_waitcnt lgkmcnt(11)
	v_fmac_f32_e32 v82, v71, v241
	v_fmac_f32_e32 v82, v70, v240
	v_fmac_f32_e32 v82, v69, v243
	v_fmac_f32_e32 v82, v68, v242
	ds_read_b128 v[240:243], v39 offset:10240
	s_waitcnt lgkmcnt(11)
	v_fmac_f32_e32 v80, v71, v245
	v_fmac_f32_e32 v80, v70, v244
	v_fmac_f32_e32 v80, v69, v247
	v_fmac_f32_e32 v80, v68, v246
	ds_read_b128 v[244:247], v39 offset:14336
	s_waitcnt lgkmcnt(11)
	v_fmac_f32_e32 v78, v71, v119
	v_fmac_f32_e32 v78, v70, v118
	v_fmac_f32_e32 v78, v69, v121
	v_fmac_f32_e32 v78, v68, v120
	ds_read_b128 v[118:121], v39 offset:18432
	s_waitcnt lgkmcnt(11)
	v_fmac_f32_e32 v76, v71, v123
	v_fmac_f32_e32 v76, v70, v122
	v_fmac_f32_e32 v76, v69, v125
	v_fmac_f32_e32 v76, v68, v124
	ds_read_b128 v[122:125], v39 offset:22528
	s_waitcnt lgkmcnt(11)
	v_mul_f32_e32 v83, v71, v127
	v_fmac_f32_e32 v83, v70, v126
	v_mul_f32_e32 v88, v69, v129
	v_fmac_f32_e32 v88, v68, v128
	ds_read_b128 v[126:129], v39 offset:26624
	v_add_f32_e32 v83, v83, v88
	v_add_f32_e32 v88, v74, v83
	s_waitcnt lgkmcnt(11)
	v_fma_f32 v90, v69, v133, v37
	v_fmac_f32_e32 v90, v68, v132
	v_fmac_f32_e32 v90, v71, v131
	v_fmac_f32_e32 v90, v70, v130
	ds_read_b128 v[130:133], v39 offset:30720
	s_waitcnt lgkmcnt(11)
	v_fma_f32 v92, v69, v137, v36
	v_fmac_f32_e32 v92, v68, v136
	v_fmac_f32_e32 v92, v71, v135
	v_fmac_f32_e32 v92, v70, v134
	ds_read_b128 v[134:137], v39 offset:34816
	s_waitcnt lgkmcnt(11)
; #define LAS __attribute__((address_space(3)))
; __device__ __forceinline__ void ph_ln1(const Params& p, int l, LAS unsigned char* lds, const int wvid) {
;     ...
; #pragma unroll
;         for (int j = 0; j < 4; ++j)
; #pragma unroll
;             for (int e = 0; e < 16; ++e) { const f32x4 w = *(const LAS f32x4*)(rw + e * D + 256 * j + 4 * lane);
;                 lg[e] += (v[j][0] * w[0] + v[j][1] * w[1]) + (v[j][2] * w[2] + v[j][3] * w[3]); }
	v_fma_f32 v93, v71, v139, v35
	v_fmac_f32_e32 v93, v69, v141
	v_fmac_f32_e32 v93, v70, v138
	v_fmac_f32_e32 v93, v68, v140
	ds_read_b128 v[138:141], v39 offset:38912
	s_waitcnt lgkmcnt(11)
	v_fma_f32 v94, v71, v143, v34
	v_fmac_f32_e32 v94, v69, v145
	v_fmac_f32_e32 v94, v70, v142
	v_fmac_f32_e32 v94, v68, v144
	ds_read_b128 v[142:145], v39 offset:43008
	s_waitcnt lgkmcnt(11)
	v_fmac_f32_e32 v0, v71, v147
	v_fmac_f32_e32 v0, v70, v146
	v_fmac_f32_e32 v0, v69, v149
	v_fmac_f32_e32 v0, v68, v148
	ds_read_b128 v[146:149], v39 offset:47104
	s_waitcnt lgkmcnt(11)
	v_fma_f32 v91, v67, v233, v72
	v_fmac_f32_e32 v91, v66, v232
	v_fmac_f32_e32 v91, v65, v235
	v_fmac_f32_e32 v91, v64, v234
	ds_read_b128 v[232:235], v39 offset:51200
	s_waitcnt lgkmcnt(11)
	v_fma_f32 v89, v67, v237, v73
	v_fmac_f32_e32 v89, v66, v236
	v_fmac_f32_e32 v89, v65, v239
	v_fmac_f32_e32 v89, v64, v238
	ds_read_b128 v[236:239], v39 offset:55296
	s_waitcnt lgkmcnt(11)
	v_fma_f32 v83, v67, v241, v75
	v_fmac_f32_e32 v83, v66, v240
	v_fmac_f32_e32 v83, v65, v243
	v_fmac_f32_e32 v83, v64, v242
	ds_read_b128 v[240:243], v39 offset:59392
	s_waitcnt lgkmcnt(11)
	v_fma_f32 v75, v67, v245, v77
	v_fmac_f32_e32 v75, v66, v244
	v_fmac_f32_e32 v75, v65, v247
	v_fmac_f32_e32 v75, v64, v246
	ds_read_b128 v[244:247], v39 offset:63488
	s_waitcnt lgkmcnt(11)
	v_fma_f32 v72, v67, v119, v79
	v_fmac_f32_e32 v72, v66, v118
	v_fmac_f32_e32 v72, v65, v121
	v_fmac_f32_e32 v72, v64, v120
	ds_read_b128 v[118:121], v39 offset:3072
	s_waitcnt lgkmcnt(11)
	v_fma_f32 v74, v67, v123, v81
	v_fmac_f32_e32 v74, v66, v122
	v_fmac_f32_e32 v74, v65, v125
	v_fmac_f32_e32 v74, v64, v124
	ds_read_b128 v[122:125], v39 offset:7168
	s_waitcnt lgkmcnt(11)
	v_fma_f32 v73, v67, v127, v82
	v_fmac_f32_e32 v73, v66, v126
	v_fmac_f32_e32 v73, v65, v129
	v_fmac_f32_e32 v73, v64, v128
	ds_read_b128 v[126:129], v39 offset:11264
	s_waitcnt lgkmcnt(11)
	v_fma_f32 v71, v67, v131, v80
	v_fmac_f32_e32 v71, v66, v130
	v_fmac_f32_e32 v71, v65, v133
	v_fmac_f32_e32 v71, v64, v132
	ds_read_b128 v[130:133], v39 offset:15360
	s_waitcnt lgkmcnt(11)
	v_fma_f32 v70, v67, v135, v78
	v_fmac_f32_e32 v70, v66, v134
	v_fmac_f32_e32 v70, v65, v137
	v_fmac_f32_e32 v70, v64, v136
	ds_read_b128 v[134:137], v39 offset:19456
	s_waitcnt lgkmcnt(11)
	v_fma_f32 v69, v67, v139, v76
	v_fmac_f32_e32 v69, v66, v138
	v_fmac_f32_e32 v69, v65, v141
	v_fmac_f32_e32 v69, v64, v140
	ds_read_b128 v[138:141], v39 offset:23552
	s_waitcnt lgkmcnt(11)
	v_fma_f32 v68, v67, v143, v88
	v_fmac_f32_e32 v68, v66, v142
	v_fmac_f32_e32 v68, v65, v145
	v_fmac_f32_e32 v68, v64, v144
	ds_read_b128 v[142:145], v39 offset:27648
	s_waitcnt lgkmcnt(11)
	v_fma_f32 v37, v67, v147, v90
	v_fmac_f32_e32 v37, v66, v146
	v_fmac_f32_e32 v37, v65, v149
	v_fmac_f32_e32 v37, v64, v148
	ds_read_b128 v[146:149], v39 offset:31744
	s_waitcnt lgkmcnt(11)
	v_fma_f32 v36, v67, v233, v92
	v_fmac_f32_e32 v36, v65, v235
	v_fmac_f32_e32 v36, v66, v232
	v_fmac_f32_e32 v36, v64, v234
	ds_read_b128 v[232:235], v39 offset:35840
	s_waitcnt lgkmcnt(11)
	v_mul_f32_e32 v34, v67, v237
	v_mul_f32_e32 v35, v65, v239
	v_fmac_f32_e32 v34, v66, v236
	v_fmac_f32_e32 v35, v64, v238
	ds_read_b128 v[236:239], v39 offset:39936
	v_add_f32_e32 v34, v34, v35
	v_add_f32_e32 v35, v93, v34
	s_waitcnt lgkmcnt(11)
	v_mul_f32_e32 v34, v67, v241
	v_fmac_f32_e32 v34, v66, v240
	v_mul_f32_e32 v76, v65, v243
	v_fmac_f32_e32 v76, v64, v242
	ds_read_b128 v[240:243], v39 offset:44032
	v_add_f32_e32 v34, v34, v76
	v_add_f32_e32 v34, v94, v34
	s_waitcnt lgkmcnt(11)
	v_mul_f32_e32 v67, v67, v245
	v_mul_f32_e32 v65, v65, v247
	v_fmac_f32_e32 v67, v66, v244
	v_fmac_f32_e32 v65, v64, v246
	ds_read_b128 v[244:247], v39 offset:48128
	v_add_f32_e32 v64, v67, v65
	v_add_f32_e32 v0, v0, v64
	s_waitcnt lgkmcnt(11)
	v_mul_f32_e32 v65, v63, v119
	v_fmac_f32_e32 v65, v62, v118
	v_mul_f32_e32 v64, v61, v121
	v_fmac_f32_e32 v64, v60, v120
	ds_read_b128 v[118:121], v39 offset:52224
	v_add_f32_e32 v64, v65, v64
	s_waitcnt lgkmcnt(11)
	v_mul_f32_e32 v65, v63, v123
	v_mul_f32_e32 v66, v61, v125
	v_fmac_f32_e32 v65, v62, v122
	v_fmac_f32_e32 v66, v60, v124
	ds_read_b128 v[122:125], v39 offset:56320
	v_add_f32_e32 v65, v65, v66
	v_add_f32_e32 v64, v91, v64
	v_add_f32_e32 v65, v89, v65
	s_waitcnt lgkmcnt(11)
	v_mul_f32_e32 v66, v63, v127
	v_mul_f32_e32 v67, v61, v129
	v_fmac_f32_e32 v66, v62, v126
	v_fmac_f32_e32 v67, v60, v128
	ds_read_b128 v[126:129], v39 offset:60416
	v_add_f32_e32 v66, v66, v67
	v_add_f32_e32 v66, v83, v66
	s_waitcnt lgkmcnt(11)
	v_mul_f32_e32 v67, v63, v131
	v_fmac_f32_e32 v67, v62, v130
	v_mul_f32_e32 v76, v61, v133
	v_fmac_f32_e32 v76, v60, v132
	ds_read_b128 v[130:133], v39 offset:64512
	v_add_f32_e32 v67, v67, v76
	v_add_f32_e32 v67, v75, v67
	s_waitcnt lgkmcnt(11)
; #define LAS __attribute__((address_space(3)))
; template <int CTRL> __device__ __forceinline__ float dpp_get(float v) { return __int_as_float(__builtin_amdgcn_update_dpp(0, __float_as_int(v), CTRL, 0xF, 0xF, false)); }
; __device__ __forceinline__ void ph_ln1(const Params& p, int l, LAS unsigned char* lds, const int wvid) {
;     ...
;         for (int j = 0; j < 4; ++j)
; #pragma unroll
;             for (int e = 0; e < 16; ++e) { const f32x4 w = *(const LAS f32x4*)(rw + e * D + 256 * j + 4 * lane);
;                 lg[e] += (v[j][0] * w[0] + v[j][1] * w[1]) + (v[j][2] * w[2] + v[j][3] * w[3]); }
;         { const bool b3 = lane & 8, b2 = lane & 4, b1 = lane & 2, b0 = lane & 1;
;           float h8[8], h4[4], h2[2];
; #pragma unroll
;           for (int i = 0; i < 8; ++i) h8[i] = (b3 ? lg[i + 8] : lg[i]) + dpp_get<0x128>(b3 ? lg[i] : lg[i + 8]);
; #pragma unroll
;           for (int i = 0; i < 4; ++i) h4[i] = (b2 ? h8[i + 4] : h8[i]) + dpp_get<0x141>(b2 ? h8[i] : h8[i + 4]);
; #pragma unroll
;           for (int i = 0; i < 2; ++i) h2[i] = (b1 ? h4[i + 2] : h4[i]) + dpp_get<0x4E>(b1 ? h4[i] : h4[i + 2]);
;           float x = (b0 ? h2[1] : h2[0]) + dpp_get<0xB1>(b0 ? h2[0] : h2[1]);
;           x += __shfl_xor(x, 16); x += __shfl_xor(x, 32);
;           if (lane < 16) LG[(wave * 20 + k) * 16 + lane] = x; }
	v_fmac_f32_e32 v72, v63, v135
	v_fmac_f32_e32 v72, v62, v134
	v_fmac_f32_e32 v72, v61, v137
	v_fmac_f32_e32 v72, v60, v136
	s_waitcnt lgkmcnt(10)
	v_fmac_f32_e32 v74, v63, v139
	v_fmac_f32_e32 v74, v62, v138
	v_fmac_f32_e32 v74, v61, v141
	v_fmac_f32_e32 v74, v60, v140
	s_waitcnt lgkmcnt(9)
	v_fmac_f32_e32 v73, v63, v143
	v_fmac_f32_e32 v73, v62, v142
	v_fmac_f32_e32 v73, v61, v145
	v_fmac_f32_e32 v73, v60, v144
	s_waitcnt lgkmcnt(8)
	v_fmac_f32_e32 v71, v63, v147
	v_fmac_f32_e32 v71, v62, v146
	v_fmac_f32_e32 v71, v61, v149
	v_fmac_f32_e32 v71, v60, v148
	s_waitcnt lgkmcnt(7)
	v_fmac_f32_e32 v70, v63, v233
	v_fmac_f32_e32 v70, v62, v232
	v_fmac_f32_e32 v70, v61, v235
	v_fmac_f32_e32 v70, v60, v234
	s_waitcnt lgkmcnt(6)
	v_fmac_f32_e32 v69, v63, v237
	v_fmac_f32_e32 v69, v62, v236
	v_fmac_f32_e32 v69, v61, v239
	v_fmac_f32_e32 v69, v60, v238
	s_waitcnt lgkmcnt(5)
	v_fmac_f32_e32 v68, v63, v241
	v_fmac_f32_e32 v68, v62, v240
	v_fmac_f32_e32 v68, v61, v243
	v_fmac_f32_e32 v68, v60, v242
	s_waitcnt lgkmcnt(4)
	v_mul_f32_e32 v75, v63, v245
	v_fmac_f32_e32 v75, v62, v244
	v_mul_f32_e32 v76, v61, v247
	v_fmac_f32_e32 v76, v60, v246
	v_add_f32_e32 v75, v75, v76
	v_add_f32_e32 v75, v37, v75
	s_waitcnt lgkmcnt(3)
	v_fma_f32 v80, v63, v119, v36
	v_fmac_f32_e32 v80, v62, v118
	v_fmac_f32_e32 v80, v61, v121
	v_fmac_f32_e32 v80, v60, v120
	s_waitcnt lgkmcnt(2)
	v_fma_f32 v81, v63, v123, v35
	v_fmac_f32_e32 v81, v61, v125
	v_fmac_f32_e32 v81, v62, v122
	v_fmac_f32_e32 v81, v60, v124
	s_waitcnt lgkmcnt(1)
	v_fma_f32 v76, v63, v127, v34
	v_fmac_f32_e32 v76, v61, v129
	v_fmac_f32_e32 v76, v62, v126
	v_fmac_f32_e32 v76, v60, v128
	s_waitcnt lgkmcnt(0)
	v_mul_f32_e32 v35, v63, v131
	v_fmac_f32_e32 v35, v62, v130
	v_mul_f32_e32 v34, v61, v133
	v_fmac_f32_e32 v34, v60, v132
	v_add_f32_e32 v34, v35, v34
	v_add_f32_e32 v0, v0, v34
	v_cndmask_b32_e32 v34, v70, v64, vcc
	v_cndmask_b32_e32 v35, v64, v70, vcc
	v_cndmask_b32_e32 v36, v65, v69, vcc
	v_cndmask_b32_e32 v37, v66, v68, vcc
	v_add_f32_dpp v34, v35, v34 row_ror:8 row_mask:0xf bank_mask:0xf bound_ctrl:1
	v_cndmask_b32_e32 v35, v69, v65, vcc
	v_cndmask_b32_e32 v60, v67, v75, vcc
	v_cndmask_b32_e32 v61, v72, v80, vcc
	v_add_f32_dpp v35, v36, v35 row_ror:8 row_mask:0xf bank_mask:0xf bound_ctrl:1
	v_cndmask_b32_e32 v36, v68, v66, vcc
	v_cndmask_b32_e32 v62, v74, v81, vcc
	v_cndmask_b32_e32 v63, v73, v76, vcc
	v_add_f32_dpp v36, v37, v36 row_ror:8 row_mask:0xf bank_mask:0xf bound_ctrl:1
	v_cndmask_b32_e32 v37, v75, v67, vcc
	s_nop 1
	v_add_f32_dpp v37, v60, v37 row_ror:8 row_mask:0xf bank_mask:0xf bound_ctrl:1
	v_cndmask_b32_e32 v60, v80, v72, vcc
	s_nop 1
	v_add_f32_dpp v60, v61, v60 row_ror:8 row_mask:0xf bank_mask:0xf bound_ctrl:1
	v_cndmask_b32_e32 v61, v81, v74, vcc
	s_nop 1
	v_add_f32_dpp v61, v62, v61 row_ror:8 row_mask:0xf bank_mask:0xf bound_ctrl:1
	v_cndmask_b32_e32 v62, v76, v73, vcc
	s_nop 1
	v_add_f32_dpp v62, v63, v62 row_ror:8 row_mask:0xf bank_mask:0xf bound_ctrl:1
	v_cndmask_b32_e32 v63, v0, v71, vcc
	v_cndmask_b32_e32 v0, v71, v0, vcc
	s_nop 1
	v_add_f32_dpp v0, v0, v63 row_ror:8 row_mask:0xf bank_mask:0xf bound_ctrl:1
	v_cndmask_b32_e64 v63, v60, v34, s[4:5]
	v_cndmask_b32_e64 v34, v34, v60, s[4:5]
	v_cndmask_b32_e64 v60, v61, v35, s[4:5]
	v_cndmask_b32_e64 v35, v35, v61, s[4:5]
	v_add_f32_dpp v34, v34, v63 row_half_mirror row_mask:0xf bank_mask:0xf bound_ctrl:1
	s_nop 0
	v_add_f32_dpp v35, v35, v60 row_half_mirror row_mask:0xf bank_mask:0xf bound_ctrl:1
	v_cndmask_b32_e64 v60, v62, v36, s[4:5]
	v_cndmask_b32_e64 v36, v36, v62, s[4:5]
	s_nop 1
	v_add_f32_dpp v36, v36, v60 row_half_mirror row_mask:0xf bank_mask:0xf bound_ctrl:1
	v_cndmask_b32_e64 v60, v0, v37, s[4:5]
	v_cndmask_b32_e64 v0, v37, v0, s[4:5]
	v_cndmask_b32_e64 v37, v36, v34, s[6:7]
	v_cndmask_b32_e64 v34, v34, v36, s[6:7]
	v_add_f32_dpp v0, v0, v60 row_half_mirror row_mask:0xf bank_mask:0xf bound_ctrl:1
	v_cndmask_b32_e64 v36, v0, v35, s[6:7]
	v_cndmask_b32_e64 v0, v35, v0, s[6:7]
	v_add_f32_dpp v34, v34, v37 quad_perm:[2,3,0,1] row_mask:0xf bank_mask:0xf bound_ctrl:1
	s_nop 0
	v_add_f32_dpp v0, v0, v36 quad_perm:[2,3,0,1] row_mask:0xf bank_mask:0xf bound_ctrl:1
	v_cndmask_b32_e64 v35, v0, v34, s[8:9]
	v_cndmask_b32_e64 v0, v34, v0, s[8:9]
	s_nop 1
	v_add_f32_dpp v0, v0, v35 quad_perm:[1,0,3,2] row_mask:0xf bank_mask:0xf bound_ctrl:1
	ds_bpermute_b32 v34, v43, v0
	s_waitcnt lgkmcnt(0)
	v_add_f32_e32 v0, v0, v34
	ds_bpermute_b32 v34, v85, v0
	s_and_saveexec_b64 s[0:1], s[10:11]
	s_cbranch_execz .LBB0_1073
	s_waitcnt lgkmcnt(0)
	v_add_f32_e32 v0, v0, v34
	ds_write_b32 v86, v0
	s_branch .LBB0_1073
